# baseline (speedup 1.0000x reference)
_Z22k2_resolve_rank_gatherPKfS0_PKdS0_PKiPKyPKtS0_S4_Pf:
	s_load_dwordx16 s[4:19], s[0:1], 0x0
	s_load_dwordx4 s[20:23], s[0:1], 0x40
	v_and_b32_e32 v1, 0x3ff, v0
	s_lshr_b32 s24, s2, 6
	s_and_b32 s25, s2, 63
	s_lshl_b32 s26, s24, 9
	v_lshl_add_u32 v2, v1, 1, s26
	v_lshlrev_b32_e32 v3, 4, v2
	v_lshlrev_b32_e32 v24, 2, v2
	v_lshlrev_b32_e32 v25, 3, v2
	v_mov_b32_e32 v106, 0
	v_mov_b32_e32 v107, 0
	v_mov_b32_e32 v105, 0x1800
	v_lshlrev_b32_e32 v104, 3, v1
	s_movk_i32 s30, 0x641
	s_mov_b32 s32, 0xa0b5ed8d
	s_mov_b32 s33, 0x3ed0c6f7
	s_mov_b32 s34, 0xa0b5ed8d
	s_mov_b32 s35, 0xbed0c6f7
	s_mul_i32 s31, s26, 0x1904
	v_lshrrev_b32_e32 v29, 6, v1
	s_waitcnt lgkmcnt(0)
	global_load_dwordx4 v[4:7], v3, s[16:17]
	global_load_dwordx4 v[8:11], v3, s[16:17] offset:16
	global_load_dwordx2 v[12:13], v24, s[10:11]
	global_load_dwordx2 v[16:17], v24, s[12:13]
	global_load_dwordx4 v[20:23], v25, s[8:9]
	global_load_dwordx2 v[14:15], v24, s[18:19]
	global_load_dwordx2 v[18:19], v24, s[20:21]
	s_add_u32 s28, s4, s31
	s_addc_u32 s29, s5, 0
	v_readfirstlane_b32 s27, v29
	ds_write_b64 v105, v[106:107]
	ds_write_b64 v105, v[106:107] offset:8
	ds_write_b64 v105, v[106:107] offset:16
	ds_write_b64 v105, v[106:107] offset:24
	ds_write_b64 v104, v[106:107] offset:8448
	s_mov_b64 s[36:37], 0
	s_mov_b64 s[38:39], 0
	s_mov_b64 s[40:41], 0
	s_mov_b64 s[42:43], 0
	s_mov_b64 s[44:45], 0
	v_lshlrev_b32_e32 v2, 4, v1
	s_waitcnt vmcnt(2)
	ds_write_b128 v2, v[20:23] offset:12544
	v_lshlrev_b32_e32 v3, 5, v1
	ds_write_b128 v3, v[4:7] offset:22784
	ds_write_b128 v3, v[8:11] offset:22800
	ds_write_b64 v104, v[16:17] offset:30976
	v_and_b32_e32 v26, 0xffff, v4
	v_and_b32_e32 v27, 0xffff, v8
	v_max_u32_e32 v28, v26, v27
	v_cvt_f64_f32_e32 v[92:93], v12
	v_cvt_f64_f32_e32 v[94:95], v13
	v_add_f64 v[92:93], v[92:93], -v[20:21]
	v_add_f64 v[94:95], v[94:95], -v[22:23]
	ds_write_b128 v2, v[92:95] offset:0
	ds_write_b64 v104, v[12:13] offset:4096
	s_waitcnt vmcnt(0)
	ds_write_b64 v104, v[14:15] offset:33024
	v_cvt_f64_f32_e32 v[96:97], v14
	v_cvt_f64_f32_e32 v[98:99], v15
	v_add_f64 v[96:97], v[96:97], -v[20:21]
	v_add_f64 v[98:99], v[98:99], -v[22:23]
	s_waitcnt lgkmcnt(0)
	s_barrier
	v_cmp_lt_u32_e32 vcc, 0, v28
	s_cbranch_vccz .Lk2_l1_done
	v_cmp_lt_u32_e32 vcc, 0, v26
	s_and_saveexec_b64 s[46:47], vcc
	s_cbranch_execz .Lk2_l1_0_0
	v_lshrrev_b32_e32 v29, 16, v4
	v_mad_u32_u24 v30, v29, s30, v16
	v_mad_u32_u24 v31, v29, s30, v18
	v_lshlrev_b32_e32 v30, 2, v30
	v_lshlrev_b32_e32 v31, 2, v31
	global_load_dword v88, v30, s[28:29]
	global_load_dword v89, v31, s[28:29]
.Lk2_l1_0_0:
	s_or_b64 exec, exec, s[46:47]
	v_cmp_lt_u32_e32 vcc, 0, v27
	s_and_saveexec_b64 s[46:47], vcc
	s_cbranch_execz .Lk2_l1_0_1
	v_lshrrev_b32_e32 v29, 16, v8
	v_mad_u32_u24 v30, v29, s30, v17
	v_mad_u32_u24 v31, v29, s30, v19
	v_lshlrev_b32_e32 v30, 2, v30
	v_lshlrev_b32_e32 v31, 2, v31
	global_load_dword v90, v30, s[28:29]
	global_load_dword v91, v31, s[28:29]
.Lk2_l1_0_1:
	s_or_b64 exec, exec, s[46:47]
	v_cmp_lt_u32_e32 vcc, 1, v28
	s_cbranch_vccz .Lk2_l1_done
	v_cmp_lt_u32_e32 vcc, 1, v26
	s_and_saveexec_b64 s[46:47], vcc
	s_cbranch_execz .Lk2_l1_1_0
	v_and_b32_e32 v29, 0xffff, v5
	v_mad_u32_u24 v30, v29, s30, v16
	v_mad_u32_u24 v31, v29, s30, v18
	v_lshlrev_b32_e32 v30, 2, v30
	v_lshlrev_b32_e32 v31, 2, v31
	global_load_dword v100, v30, s[28:29]
	global_load_dword v101, v31, s[28:29]
.Lk2_l1_1_0:
	s_or_b64 exec, exec, s[46:47]
	v_cmp_lt_u32_e32 vcc, 1, v27
	s_and_saveexec_b64 s[46:47], vcc
	s_cbranch_execz .Lk2_l1_1_1
	v_and_b32_e32 v29, 0xffff, v9
	v_mad_u32_u24 v30, v29, s30, v17
	v_mad_u32_u24 v31, v29, s30, v19
	v_lshlrev_b32_e32 v30, 2, v30
	v_lshlrev_b32_e32 v31, 2, v31
	global_load_dword v102, v30, s[28:29]
	global_load_dword v103, v31, s[28:29]
.Lk2_l1_1_1:
	s_or_b64 exec, exec, s[46:47]
	v_cmp_lt_u32_e32 vcc, 2, v28
	s_cbranch_vccz .Lk2_l1_done
	v_cmp_lt_u32_e32 vcc, 2, v26
	s_and_saveexec_b64 s[46:47], vcc
	s_cbranch_execz .Lk2_l1_2_0
	v_lshrrev_b32_e32 v29, 16, v5
	v_mad_u32_u24 v30, v29, s30, v16
	v_mad_u32_u24 v31, v29, s30, v18
	v_lshlrev_b32_e32 v30, 2, v30
	v_lshlrev_b32_e32 v31, 2, v31
	global_load_dword v108, v30, s[28:29]
	global_load_dword v109, v31, s[28:29]
.Lk2_l1_2_0:
	s_or_b64 exec, exec, s[46:47]
	v_cmp_lt_u32_e32 vcc, 2, v27
	s_and_saveexec_b64 s[46:47], vcc
	s_cbranch_execz .Lk2_l1_2_1
	v_lshrrev_b32_e32 v29, 16, v9
	v_mad_u32_u24 v30, v29, s30, v17
	v_mad_u32_u24 v31, v29, s30, v19
	v_lshlrev_b32_e32 v30, 2, v30
	v_lshlrev_b32_e32 v31, 2, v31
	global_load_dword v110, v30, s[28:29]
	global_load_dword v111, v31, s[28:29]
.Lk2_l1_2_1:
	s_or_b64 exec, exec, s[46:47]
	v_cmp_lt_u32_e32 vcc, 3, v28
	s_cbranch_vccz .Lk2_l1_done
	v_cmp_lt_u32_e32 vcc, 3, v26
	s_and_saveexec_b64 s[46:47], vcc
	s_cbranch_execz .Lk2_l1_3_0
	v_and_b32_e32 v29, 0xffff, v6
	v_mad_u32_u24 v30, v29, s30, v16
	v_mad_u32_u24 v31, v29, s30, v18
	v_lshlrev_b32_e32 v30, 2, v30
	v_lshlrev_b32_e32 v31, 2, v31
	global_load_dword v112, v30, s[28:29]
	global_load_dword v113, v31, s[28:29]
.Lk2_l1_3_0:
	s_or_b64 exec, exec, s[46:47]
	v_cmp_lt_u32_e32 vcc, 3, v27
	s_and_saveexec_b64 s[46:47], vcc
	s_cbranch_execz .Lk2_l1_3_1
	v_and_b32_e32 v29, 0xffff, v10
	v_mad_u32_u24 v30, v29, s30, v17
	v_mad_u32_u24 v31, v29, s30, v19
	v_lshlrev_b32_e32 v30, 2, v30
	v_lshlrev_b32_e32 v31, 2, v31
	global_load_dword v114, v30, s[28:29]
	global_load_dword v115, v31, s[28:29]
.Lk2_l1_3_1:
	s_or_b64 exec, exec, s[46:47]
	v_cmp_lt_u32_e32 vcc, 4, v28
	s_cbranch_vccz .Lk2_l1_done
	v_cmp_lt_u32_e32 vcc, 4, v26
	s_and_saveexec_b64 s[46:47], vcc
	s_cbranch_execz .Lk2_l1_4_0
	v_lshrrev_b32_e32 v29, 16, v6
	v_mad_u32_u24 v30, v29, s30, v16
	v_mad_u32_u24 v31, v29, s30, v18
	v_lshlrev_b32_e32 v30, 2, v30
	v_lshlrev_b32_e32 v31, 2, v31
	global_load_dword v116, v30, s[28:29]
	global_load_dword v117, v31, s[28:29]
.Lk2_l1_4_0:
	s_or_b64 exec, exec, s[46:47]
	v_cmp_lt_u32_e32 vcc, 4, v27
	s_and_saveexec_b64 s[46:47], vcc
	s_cbranch_execz .Lk2_l1_4_1
	v_lshrrev_b32_e32 v29, 16, v10
	v_mad_u32_u24 v30, v29, s30, v17
	v_mad_u32_u24 v31, v29, s30, v19
	v_lshlrev_b32_e32 v30, 2, v30
	v_lshlrev_b32_e32 v31, 2, v31
	global_load_dword v118, v30, s[28:29]
	global_load_dword v119, v31, s[28:29]
.Lk2_l1_4_1:
	s_or_b64 exec, exec, s[46:47]
	v_cmp_lt_u32_e32 vcc, 5, v28
	s_cbranch_vccz .Lk2_l1_done
	v_cmp_lt_u32_e32 vcc, 5, v26
	s_and_saveexec_b64 s[46:47], vcc
	s_cbranch_execz .Lk2_l1_5_0
	v_and_b32_e32 v29, 0xffff, v7
	v_mad_u32_u24 v30, v29, s30, v16
	v_mad_u32_u24 v31, v29, s30, v18
	v_lshlrev_b32_e32 v30, 2, v30
	v_lshlrev_b32_e32 v31, 2, v31
	global_load_dword v120, v30, s[28:29]
	global_load_dword v121, v31, s[28:29]
.Lk2_l1_5_0:
	s_or_b64 exec, exec, s[46:47]
	v_cmp_lt_u32_e32 vcc, 5, v27
	s_and_saveexec_b64 s[46:47], vcc
	s_cbranch_execz .Lk2_l1_5_1
	v_and_b32_e32 v29, 0xffff, v11
	v_mad_u32_u24 v30, v29, s30, v17
	v_mad_u32_u24 v31, v29, s30, v19
	v_lshlrev_b32_e32 v30, 2, v30
	v_lshlrev_b32_e32 v31, 2, v31
	global_load_dword v122, v30, s[28:29]
	global_load_dword v123, v31, s[28:29]
.Lk2_l1_5_1:
	s_or_b64 exec, exec, s[46:47]
	v_cmp_lt_u32_e32 vcc, 6, v28
	s_cbranch_vccz .Lk2_l1_done
	v_cmp_lt_u32_e32 vcc, 6, v26
	s_and_saveexec_b64 s[46:47], vcc
	s_cbranch_execz .Lk2_l1_6_0
	v_lshrrev_b32_e32 v29, 16, v7
	v_mad_u32_u24 v30, v29, s30, v16
	v_mad_u32_u24 v31, v29, s30, v18
	v_lshlrev_b32_e32 v30, 2, v30
	v_lshlrev_b32_e32 v31, 2, v31
	global_load_dword v124, v30, s[28:29]
	global_load_dword v125, v31, s[28:29]
.Lk2_l1_6_0:
	s_or_b64 exec, exec, s[46:47]
	v_cmp_lt_u32_e32 vcc, 6, v27
	s_and_saveexec_b64 s[46:47], vcc
	s_cbranch_execz .Lk2_l1_6_1
	v_lshrrev_b32_e32 v29, 16, v11
	v_mad_u32_u24 v30, v29, s30, v17
	v_mad_u32_u24 v31, v29, s30, v19
	v_lshlrev_b32_e32 v30, 2, v30
	v_lshlrev_b32_e32 v31, 2, v31
	global_load_dword v126, v30, s[28:29]
	global_load_dword v127, v31, s[28:29]

.Lk2_l1_done:
	v_lshrrev_b32_e32 v29, 5, v1
	v_and_b32_e32 v31, 31, v1
	v_lshl_add_u32 v29, s25, 3, v29
	v_lshlrev_b32_e32 v29, 3, v29
	v_lshlrev_b32_e32 v31, 3, v31
	ds_read_b64 v[64:65], v29 offset:0
	ds_read_b64 v[32:33], v31 offset:0
	ds_read_b64 v[34:35], v31 offset:256
	ds_read_b64 v[36:37], v31 offset:512
	ds_read_b64 v[38:39], v31 offset:768
	ds_read_b64 v[40:41], v31 offset:1024
	ds_read_b64 v[42:43], v31 offset:1280
	ds_read_b64 v[44:45], v31 offset:1536
	ds_read_b64 v[46:47], v31 offset:1792
	ds_read_b64 v[48:49], v31 offset:2048
	ds_read_b64 v[50:51], v31 offset:2304
	ds_read_b64 v[52:53], v31 offset:2560
	ds_read_b64 v[54:55], v31 offset:2816
	ds_read_b64 v[56:57], v31 offset:3072
	v_mov_b32_e32 v66, 0
	v_mov_b32_e32 v67, 0
	s_waitcnt lgkmcnt(12)
	ds_read_b64 v[58:59], v31 offset:3328
	v_add_f64 v[70:71], v[32:33], -v[64:65]
	v_cmp_lt_f64_e32 vcc, s[32:33], v[70:71]
	v_cmp_ge_f64_e64 s[48:49], s[32:33], |v[70:71]|
	s_nop 0
	v_addc_co_u32_e32 v66, vcc, 0, v66, vcc
	v_addc_co_u32_e64 v67, s[50:51], 0, v67, s[48:49]
	s_waitcnt lgkmcnt(12)
	ds_read_b64 v[60:61], v31 offset:3584
	v_add_f64 v[70:71], v[34:35], -v[64:65]
	v_cmp_lt_f64_e32 vcc, s[32:33], v[70:71]
	v_cmp_ge_f64_e64 s[48:49], s[32:33], |v[70:71]|
	s_nop 0
	v_addc_co_u32_e32 v66, vcc, 0, v66, vcc
	v_addc_co_u32_e64 v67, s[50:51], 0, v67, s[48:49]
	s_waitcnt lgkmcnt(12)
	ds_read_b64 v[62:63], v31 offset:3840
	v_add_f64 v[70:71], v[36:37], -v[64:65]
	v_cmp_lt_f64_e32 vcc, s[32:33], v[70:71]
	v_cmp_ge_f64_e64 s[48:49], s[32:33], |v[70:71]|
	s_nop 0
	v_addc_co_u32_e32 v66, vcc, 0, v66, vcc
	v_addc_co_u32_e64 v67, s[50:51], 0, v67, s[48:49]
	s_waitcnt lgkmcnt(12)
	v_add_f64 v[70:71], v[38:39], -v[64:65]
	v_cmp_lt_f64_e32 vcc, s[32:33], v[70:71]
	v_cmp_ge_f64_e64 s[48:49], s[32:33], |v[70:71]|
	s_nop 0
	v_addc_co_u32_e32 v66, vcc, 0, v66, vcc
	v_addc_co_u32_e64 v67, s[50:51], 0, v67, s[48:49]
	s_waitcnt lgkmcnt(11)
	v_add_f64 v[70:71], v[40:41], -v[64:65]
	v_cmp_lt_f64_e32 vcc, s[32:33], v[70:71]
	v_cmp_ge_f64_e64 s[48:49], s[32:33], |v[70:71]|
	s_nop 0
	v_addc_co_u32_e32 v66, vcc, 0, v66, vcc
	v_addc_co_u32_e64 v67, s[50:51], 0, v67, s[48:49]
	s_waitcnt lgkmcnt(10)
	v_add_f64 v[70:71], v[42:43], -v[64:65]
	v_cmp_lt_f64_e32 vcc, s[32:33], v[70:71]
	v_cmp_ge_f64_e64 s[48:49], s[32:33], |v[70:71]|
	s_nop 0
	v_addc_co_u32_e32 v66, vcc, 0, v66, vcc
	v_addc_co_u32_e64 v67, s[50:51], 0, v67, s[48:49]
	s_waitcnt lgkmcnt(9)
	v_add_f64 v[70:71], v[44:45], -v[64:65]
	v_cmp_lt_f64_e32 vcc, s[32:33], v[70:71]
	v_cmp_ge_f64_e64 s[48:49], s[32:33], |v[70:71]|
	s_nop 0
	v_addc_co_u32_e32 v66, vcc, 0, v66, vcc
	v_addc_co_u32_e64 v67, s[50:51], 0, v67, s[48:49]
	s_waitcnt lgkmcnt(8)
	v_add_f64 v[70:71], v[46:47], -v[64:65]
	v_cmp_lt_f64_e32 vcc, s[32:33], v[70:71]
	v_cmp_ge_f64_e64 s[48:49], s[32:33], |v[70:71]|
	s_nop 0
	v_addc_co_u32_e32 v66, vcc, 0, v66, vcc
	v_addc_co_u32_e64 v67, s[50:51], 0, v67, s[48:49]
	s_waitcnt lgkmcnt(7)
	v_add_f64 v[70:71], v[48:49], -v[64:65]
	v_cmp_lt_f64_e32 vcc, s[32:33], v[70:71]
	v_cmp_ge_f64_e64 s[48:49], s[32:33], |v[70:71]|
	s_nop 0
	v_addc_co_u32_e32 v66, vcc, 0, v66, vcc
	v_addc_co_u32_e64 v67, s[50:51], 0, v67, s[48:49]
	s_waitcnt lgkmcnt(6)
	v_add_f64 v[70:71], v[50:51], -v[64:65]
	v_cmp_lt_f64_e32 vcc, s[32:33], v[70:71]
	v_cmp_ge_f64_e64 s[48:49], s[32:33], |v[70:71]|
	s_nop 0
	v_addc_co_u32_e32 v66, vcc, 0, v66, vcc
	v_addc_co_u32_e64 v67, s[50:51], 0, v67, s[48:49]
	s_waitcnt lgkmcnt(5)
	v_add_f64 v[70:71], v[52:53], -v[64:65]
	v_cmp_lt_f64_e32 vcc, s[32:33], v[70:71]
	v_cmp_ge_f64_e64 s[48:49], s[32:33], |v[70:71]|
	s_nop 0
	v_addc_co_u32_e32 v66, vcc, 0, v66, vcc
	v_addc_co_u32_e64 v67, s[50:51], 0, v67, s[48:49]
	s_waitcnt lgkmcnt(4)
	v_add_f64 v[70:71], v[54:55], -v[64:65]
	v_cmp_lt_f64_e32 vcc, s[32:33], v[70:71]
	v_cmp_ge_f64_e64 s[48:49], s[32:33], |v[70:71]|
	s_nop 0
	v_addc_co_u32_e32 v66, vcc, 0, v66, vcc
	v_addc_co_u32_e64 v67, s[50:51], 0, v67, s[48:49]
	s_waitcnt lgkmcnt(3)
	v_add_f64 v[70:71], v[56:57], -v[64:65]
	v_cmp_lt_f64_e32 vcc, s[32:33], v[70:71]
	v_cmp_ge_f64_e64 s[48:49], s[32:33], |v[70:71]|
	s_nop 0
	v_addc_co_u32_e32 v66, vcc, 0, v66, vcc
	v_addc_co_u32_e64 v67, s[50:51], 0, v67, s[48:49]
	s_waitcnt lgkmcnt(2)
	v_add_f64 v[70:71], v[58:59], -v[64:65]
	v_cmp_lt_f64_e32 vcc, s[32:33], v[70:71]
	v_cmp_ge_f64_e64 s[48:49], s[32:33], |v[70:71]|
	s_nop 0
	v_addc_co_u32_e32 v66, vcc, 0, v66, vcc
	v_addc_co_u32_e64 v67, s[50:51], 0, v67, s[48:49]
	s_waitcnt lgkmcnt(1)
	v_add_f64 v[70:71], v[60:61], -v[64:65]
	v_cmp_lt_f64_e32 vcc, s[32:33], v[70:71]
	v_cmp_ge_f64_e64 s[48:49], s[32:33], |v[70:71]|
	s_nop 0
	v_addc_co_u32_e32 v66, vcc, 0, v66, vcc
	v_addc_co_u32_e64 v67, s[50:51], 0, v67, s[48:49]
	s_waitcnt lgkmcnt(0)
	v_add_f64 v[70:71], v[62:63], -v[64:65]
	v_cmp_lt_f64_e32 vcc, s[32:33], v[70:71]
	v_cmp_ge_f64_e64 s[48:49], s[32:33], |v[70:71]|
	s_nop 0
	v_addc_co_u32_e32 v66, vcc, 0, v66, vcc
	v_addc_co_u32_e64 v67, s[50:51], 0, v67, s[48:49]
	v_lshl_or_b32 v68, v67, 16, v66
	s_nop 1
	v_add_u32_dpp v68, v68, v68 quad_perm:[1,0,3,2] row_mask:0xf bank_mask:0xf
	s_nop 1
	v_add_u32_dpp v68, v68, v68 quad_perm:[2,3,0,1] row_mask:0xf bank_mask:0xf
	s_nop 1
	v_add_u32_dpp v68, v68, v68 row_half_mirror row_mask:0xf bank_mask:0xf
	s_nop 1
	v_add_u32_dpp v68, v68, v68 row_mirror row_mask:0xf bank_mask:0xf
	s_nop 1
	v_add_u32_dpp v68, v68, v68 row_bcast:15 row_mask:0xa bank_mask:0xf
	s_nop 1
	v_readlane_b32 s52, v68, 31
	v_readlane_b32 s53, v68, 63
	s_and_b32 s54, s52, 0xffff
	s_lshr_b32 s55, s52, 16
	s_and_b32 s56, s53, 0xffff
	s_lshr_b32 s57, s53, 16
	s_cmp_gt_u32 s55, 1
	s_cselect_b32 s58, 1, 0
	s_cmp_lt_u32 s54, 0x64
	s_cselect_b32 s59, 1, 0
	s_and_b32 s58, s58, s59
	s_cmp_gt_u32 s57, 1
	s_cselect_b32 s60, 1, 0
	s_cmp_lt_u32 s56, 0x64
	s_cselect_b32 s61, 1, 0
	s_and_b32 s60, s60, s61
	s_or_b32 s61, s58, s60
	v_and_b32_e32 v69, 63, v1
	v_lshlrev_b32_e32 v69, 4, v69
	v_add_u32_e32 v70, 0x1000, v69
	s_lshl_b32 s62, s25, 3
	s_lshl_b32 s63, s27, 1
	s_add_u32 s62, s62, s63
	s_add_u32 s62, s62, s26
	s_lshl_b32 s62, s62, 13
	s_add_u32 s64, s6, s62
	s_addc_u32 s65, s7, 0
	s_add_u32 s66, s64, 0x2000
	s_addc_u32 s67, s65, 0
	s_mov_b32 s96, 0
	s_mov_b32 s97, 0
	s_cmp_lt_u32 s54, 0x64
	s_cbranch_scc1 .Lk2_eg_go
	s_cmp_lt_u32 s56, 0x64
	s_cbranch_scc0 .Lk2_eg_none
	s_mov_b32 s3, s54
	s_mov_b32 s54, s56
	s_mov_b32 s56, s3
	s_mov_b32 s3, s55
	s_mov_b32 s55, s57
	s_mov_b32 s57, s3
	s_mov_b32 s3, s58
	s_mov_b32 s58, s60
	s_mov_b32 s60, s3
	s_mov_b32 s3, s64
	s_mov_b32 s64, s66
	s_mov_b32 s66, s3
	s_mov_b32 s3, s65
	s_mov_b32 s65, s67
	s_mov_b32 s67, s3
	s_mov_b32 s97, 1
.Lk2_eg_go:
	s_mov_b32 s96, 1
	global_load_dwordx4 v[32:35], v69, s[64:65] offset:0 nt
	global_load_dwordx4 v[36:39], v69, s[64:65] offset:1024 nt
	global_load_dwordx4 v[40:43], v69, s[64:65] offset:2048 nt
	global_load_dwordx4 v[44:47], v69, s[64:65] offset:3072 nt
	global_load_dwordx4 v[48:51], v70, s[64:65] offset:0 nt
	global_load_dwordx4 v[52:55], v70, s[64:65] offset:1024 nt
	global_load_dwordx4 v[56:59], v70, s[64:65] offset:2048 nt
	global_load_dwordx4 v[60:63], v70, s[64:65] offset:3072 nt
	s_waitcnt vmcnt(8)
	s_branch .Lk2_eg_done

.Lk2_eg_done:
	v_cmp_lt_u32_e32 vcc, 0, v28
	s_cbranch_vccz .Lk2_l2_done
	v_cmp_lt_u32_e32 vcc, 0, v26
	s_and_saveexec_b64 s[46:47], vcc
	v_lshrrev_b32_e32 v29, 16, v4
	v_lshlrev_b32_e32 v29, 3, v29
	ds_read_b64 v[72:73], v29 offset:12544
	s_mov_b64 exec, s[46:47]
	v_cmp_lt_u32_e32 vcc, 0, v27
	s_and_saveexec_b64 s[46:47], vcc
	v_lshrrev_b32_e32 v29, 16, v8
	v_lshlrev_b32_e32 v29, 3, v29
	ds_read_b64 v[74:75], v29 offset:12544
	s_mov_b64 exec, s[46:47]
	s_waitcnt lgkmcnt(0)
	v_cmp_lt_u32_e32 vcc, 0, v26
	s_and_saveexec_b64 s[46:47], vcc
	s_cbranch_execz .Lk2_l2_0_0
	v_cvt_f64_f32_e32 v[24:25], v88
	v_cvt_f64_f32_e32 v[30:31], v89
	v_add_f64 v[24:25], v[24:25], -v[72:73]
	v_add_f64 v[30:31], v[30:31], -v[72:73]
	v_add_f64 v[24:25], v[24:25], -v[92:93]
	v_add_f64 v[30:31], v[30:31], -v[96:97]
	v_cmp_le_f64_e32 vcc, s[34:35], v[24:25]
	v_cmp_ge_f64_e64 s[48:49], s[32:33], v[24:25]
	s_or_b64 s[36:37], s[36:37], vcc
	s_and_b64 s[48:49], s[48:49], vcc
	s_or_b64 s[44:45], s[44:45], s[48:49]
	v_cmp_le_f64_e32 vcc, s[34:35], v[30:31]
	v_cmp_ge_f64_e64 s[48:49], s[32:33], v[30:31]
	s_or_b64 s[38:39], s[38:39], vcc
	s_and_b64 s[48:49], s[48:49], vcc
	s_or_b64 s[44:45], s[44:45], s[48:49]
.Lk2_l2_0_0:
	s_or_b64 exec, exec, s[46:47]
	v_cmp_lt_u32_e32 vcc, 0, v27
	s_and_saveexec_b64 s[46:47], vcc
	s_cbranch_execz .Lk2_l2_0_1
	v_cvt_f64_f32_e32 v[24:25], v90
	v_cvt_f64_f32_e32 v[30:31], v91
	v_add_f64 v[24:25], v[24:25], -v[74:75]
	v_add_f64 v[30:31], v[30:31], -v[74:75]
	v_add_f64 v[24:25], v[24:25], -v[94:95]
	v_add_f64 v[30:31], v[30:31], -v[98:99]
	v_cmp_le_f64_e32 vcc, s[34:35], v[24:25]
	v_cmp_ge_f64_e64 s[48:49], s[32:33], v[24:25]
	s_or_b64 s[40:41], s[40:41], vcc
	s_and_b64 s[48:49], s[48:49], vcc
	s_or_b64 s[44:45], s[44:45], s[48:49]
	v_cmp_le_f64_e32 vcc, s[34:35], v[30:31]
	v_cmp_ge_f64_e64 s[48:49], s[32:33], v[30:31]
	s_or_b64 s[42:43], s[42:43], vcc
	s_and_b64 s[48:49], s[48:49], vcc
	s_or_b64 s[44:45], s[44:45], s[48:49]
.Lk2_l2_0_1:
	s_or_b64 exec, exec, s[46:47]
	v_cmp_lt_u32_e32 vcc, 1, v28
	s_cbranch_vccz .Lk2_l2_done
	v_cmp_lt_u32_e32 vcc, 1, v26
	s_and_saveexec_b64 s[46:47], vcc
	v_and_b32_e32 v29, 0xffff, v5
	v_lshlrev_b32_e32 v29, 3, v29
	ds_read_b64 v[72:73], v29 offset:12544
	s_mov_b64 exec, s[46:47]
	v_cmp_lt_u32_e32 vcc, 1, v27
	s_and_saveexec_b64 s[46:47], vcc
	v_and_b32_e32 v29, 0xffff, v9
	v_lshlrev_b32_e32 v29, 3, v29
	ds_read_b64 v[74:75], v29 offset:12544
	s_mov_b64 exec, s[46:47]
	s_waitcnt lgkmcnt(0)
	v_cmp_lt_u32_e32 vcc, 1, v26
	s_and_saveexec_b64 s[46:47], vcc
	s_cbranch_execz .Lk2_l2_1_0
	v_cvt_f64_f32_e32 v[24:25], v100
	v_cvt_f64_f32_e32 v[30:31], v101
	v_add_f64 v[24:25], v[24:25], -v[72:73]
	v_add_f64 v[30:31], v[30:31], -v[72:73]
	v_add_f64 v[24:25], v[24:25], -v[92:93]
	v_add_f64 v[30:31], v[30:31], -v[96:97]
	v_cmp_le_f64_e32 vcc, s[34:35], v[24:25]
	v_cmp_ge_f64_e64 s[48:49], s[32:33], v[24:25]
	s_or_b64 s[36:37], s[36:37], vcc
	s_and_b64 s[48:49], s[48:49], vcc
	s_or_b64 s[44:45], s[44:45], s[48:49]
	v_cmp_le_f64_e32 vcc, s[34:35], v[30:31]
	v_cmp_ge_f64_e64 s[48:49], s[32:33], v[30:31]
	s_or_b64 s[38:39], s[38:39], vcc
	s_and_b64 s[48:49], s[48:49], vcc
	s_or_b64 s[44:45], s[44:45], s[48:49]
.Lk2_l2_1_0:
	s_or_b64 exec, exec, s[46:47]
	v_cmp_lt_u32_e32 vcc, 1, v27
	s_and_saveexec_b64 s[46:47], vcc
	s_cbranch_execz .Lk2_l2_1_1
	v_cvt_f64_f32_e32 v[24:25], v102
	v_cvt_f64_f32_e32 v[30:31], v103
	v_add_f64 v[24:25], v[24:25], -v[74:75]
	v_add_f64 v[30:31], v[30:31], -v[74:75]
	v_add_f64 v[24:25], v[24:25], -v[94:95]
	v_add_f64 v[30:31], v[30:31], -v[98:99]
	v_cmp_le_f64_e32 vcc, s[34:35], v[24:25]
	v_cmp_ge_f64_e64 s[48:49], s[32:33], v[24:25]
	s_or_b64 s[40:41], s[40:41], vcc
	s_and_b64 s[48:49], s[48:49], vcc
	s_or_b64 s[44:45], s[44:45], s[48:49]
	v_cmp_le_f64_e32 vcc, s[34:35], v[30:31]
	v_cmp_ge_f64_e64 s[48:49], s[32:33], v[30:31]
	s_or_b64 s[42:43], s[42:43], vcc
	s_and_b64 s[48:49], s[48:49], vcc
	s_or_b64 s[44:45], s[44:45], s[48:49]
.Lk2_l2_1_1:
	s_or_b64 exec, exec, s[46:47]
	v_cmp_lt_u32_e32 vcc, 2, v28
	s_cbranch_vccz .Lk2_l2_done
	v_cmp_lt_u32_e32 vcc, 2, v26
	s_and_saveexec_b64 s[46:47], vcc
	v_lshrrev_b32_e32 v29, 16, v5
	v_lshlrev_b32_e32 v29, 3, v29
	ds_read_b64 v[72:73], v29 offset:12544
	s_mov_b64 exec, s[46:47]
	v_cmp_lt_u32_e32 vcc, 2, v27
	s_and_saveexec_b64 s[46:47], vcc
	v_lshrrev_b32_e32 v29, 16, v9
	v_lshlrev_b32_e32 v29, 3, v29
	ds_read_b64 v[74:75], v29 offset:12544
	s_mov_b64 exec, s[46:47]
	s_waitcnt lgkmcnt(0)
	v_cmp_lt_u32_e32 vcc, 2, v26
	s_and_saveexec_b64 s[46:47], vcc
	s_cbranch_execz .Lk2_l2_2_0
	v_cvt_f64_f32_e32 v[24:25], v108
	v_cvt_f64_f32_e32 v[30:31], v109
	v_add_f64 v[24:25], v[24:25], -v[72:73]
	v_add_f64 v[30:31], v[30:31], -v[72:73]
	v_add_f64 v[24:25], v[24:25], -v[92:93]
	v_add_f64 v[30:31], v[30:31], -v[96:97]
	v_cmp_le_f64_e32 vcc, s[34:35], v[24:25]
	v_cmp_ge_f64_e64 s[48:49], s[32:33], v[24:25]
	s_or_b64 s[36:37], s[36:37], vcc
	s_and_b64 s[48:49], s[48:49], vcc
	s_or_b64 s[44:45], s[44:45], s[48:49]
	v_cmp_le_f64_e32 vcc, s[34:35], v[30:31]
	v_cmp_ge_f64_e64 s[48:49], s[32:33], v[30:31]
	s_or_b64 s[38:39], s[38:39], vcc
	s_and_b64 s[48:49], s[48:49], vcc
	s_or_b64 s[44:45], s[44:45], s[48:49]
.Lk2_l2_2_0:
	s_or_b64 exec, exec, s[46:47]
	v_cmp_lt_u32_e32 vcc, 2, v27
	s_and_saveexec_b64 s[46:47], vcc
	s_cbranch_execz .Lk2_l2_2_1
	v_cvt_f64_f32_e32 v[24:25], v110
	v_cvt_f64_f32_e32 v[30:31], v111
	v_add_f64 v[24:25], v[24:25], -v[74:75]
	v_add_f64 v[30:31], v[30:31], -v[74:75]
	v_add_f64 v[24:25], v[24:25], -v[94:95]
	v_add_f64 v[30:31], v[30:31], -v[98:99]
	v_cmp_le_f64_e32 vcc, s[34:35], v[24:25]
	v_cmp_ge_f64_e64 s[48:49], s[32:33], v[24:25]
	s_or_b64 s[40:41], s[40:41], vcc
	s_and_b64 s[48:49], s[48:49], vcc
	s_or_b64 s[44:45], s[44:45], s[48:49]
	v_cmp_le_f64_e32 vcc, s[34:35], v[30:31]
	v_cmp_ge_f64_e64 s[48:49], s[32:33], v[30:31]
	s_or_b64 s[42:43], s[42:43], vcc
	s_and_b64 s[48:49], s[48:49], vcc
	s_or_b64 s[44:45], s[44:45], s[48:49]
.Lk2_l2_2_1:
	s_or_b64 exec, exec, s[46:47]
	v_cmp_lt_u32_e32 vcc, 3, v28
	s_cbranch_vccz .Lk2_l2_done
	v_cmp_lt_u32_e32 vcc, 3, v26
	s_and_saveexec_b64 s[46:47], vcc
	v_and_b32_e32 v29, 0xffff, v6
	v_lshlrev_b32_e32 v29, 3, v29
	ds_read_b64 v[72:73], v29 offset:12544
	s_mov_b64 exec, s[46:47]
	v_cmp_lt_u32_e32 vcc, 3, v27
	s_and_saveexec_b64 s[46:47], vcc
	v_and_b32_e32 v29, 0xffff, v10
	v_lshlrev_b32_e32 v29, 3, v29
	ds_read_b64 v[74:75], v29 offset:12544
	s_mov_b64 exec, s[46:47]
	s_waitcnt lgkmcnt(0)
	v_cmp_lt_u32_e32 vcc, 3, v26
	s_and_saveexec_b64 s[46:47], vcc
	s_cbranch_execz .Lk2_l2_3_0
	v_cvt_f64_f32_e32 v[24:25], v112
	v_cvt_f64_f32_e32 v[30:31], v113
	v_add_f64 v[24:25], v[24:25], -v[72:73]
	v_add_f64 v[30:31], v[30:31], -v[72:73]
	v_add_f64 v[24:25], v[24:25], -v[92:93]
	v_add_f64 v[30:31], v[30:31], -v[96:97]
	v_cmp_le_f64_e32 vcc, s[34:35], v[24:25]
	v_cmp_ge_f64_e64 s[48:49], s[32:33], v[24:25]
	s_or_b64 s[36:37], s[36:37], vcc
	s_and_b64 s[48:49], s[48:49], vcc
	s_or_b64 s[44:45], s[44:45], s[48:49]
	v_cmp_le_f64_e32 vcc, s[34:35], v[30:31]
	v_cmp_ge_f64_e64 s[48:49], s[32:33], v[30:31]
	s_or_b64 s[38:39], s[38:39], vcc
	s_and_b64 s[48:49], s[48:49], vcc
	s_or_b64 s[44:45], s[44:45], s[48:49]
.Lk2_l2_3_0:
	s_or_b64 exec, exec, s[46:47]
	v_cmp_lt_u32_e32 vcc, 3, v27
	s_and_saveexec_b64 s[46:47], vcc
	s_cbranch_execz .Lk2_l2_3_1
	v_cvt_f64_f32_e32 v[24:25], v114
	v_cvt_f64_f32_e32 v[30:31], v115
	v_add_f64 v[24:25], v[24:25], -v[74:75]
	v_add_f64 v[30:31], v[30:31], -v[74:75]
	v_add_f64 v[24:25], v[24:25], -v[94:95]
	v_add_f64 v[30:31], v[30:31], -v[98:99]
	v_cmp_le_f64_e32 vcc, s[34:35], v[24:25]
	v_cmp_ge_f64_e64 s[48:49], s[32:33], v[24:25]
	s_or_b64 s[40:41], s[40:41], vcc
	s_and_b64 s[48:49], s[48:49], vcc
	s_or_b64 s[44:45], s[44:45], s[48:49]
	v_cmp_le_f64_e32 vcc, s[34:35], v[30:31]
	v_cmp_ge_f64_e64 s[48:49], s[32:33], v[30:31]
	s_or_b64 s[42:43], s[42:43], vcc
	s_and_b64 s[48:49], s[48:49], vcc
	s_or_b64 s[44:45], s[44:45], s[48:49]
.Lk2_l2_3_1:
	s_or_b64 exec, exec, s[46:47]
	v_cmp_lt_u32_e32 vcc, 4, v28
	s_cbranch_vccz .Lk2_l2_done
	v_cmp_lt_u32_e32 vcc, 4, v26
	s_and_saveexec_b64 s[46:47], vcc
	v_lshrrev_b32_e32 v29, 16, v6
	v_lshlrev_b32_e32 v29, 3, v29
	ds_read_b64 v[72:73], v29 offset:12544
	s_mov_b64 exec, s[46:47]
	v_cmp_lt_u32_e32 vcc, 4, v27
	s_and_saveexec_b64 s[46:47], vcc
	v_lshrrev_b32_e32 v29, 16, v10
	v_lshlrev_b32_e32 v29, 3, v29
	ds_read_b64 v[74:75], v29 offset:12544
	s_mov_b64 exec, s[46:47]
	s_waitcnt lgkmcnt(0)
	v_cmp_lt_u32_e32 vcc, 4, v26
	s_and_saveexec_b64 s[46:47], vcc
	s_cbranch_execz .Lk2_l2_4_0
	v_cvt_f64_f32_e32 v[24:25], v116
	v_cvt_f64_f32_e32 v[30:31], v117
	v_add_f64 v[24:25], v[24:25], -v[72:73]
	v_add_f64 v[30:31], v[30:31], -v[72:73]
	v_add_f64 v[24:25], v[24:25], -v[92:93]
	v_add_f64 v[30:31], v[30:31], -v[96:97]
	v_cmp_le_f64_e32 vcc, s[34:35], v[24:25]
	v_cmp_ge_f64_e64 s[48:49], s[32:33], v[24:25]
	s_or_b64 s[36:37], s[36:37], vcc
	s_and_b64 s[48:49], s[48:49], vcc
	s_or_b64 s[44:45], s[44:45], s[48:49]
	v_cmp_le_f64_e32 vcc, s[34:35], v[30:31]
	v_cmp_ge_f64_e64 s[48:49], s[32:33], v[30:31]
	s_or_b64 s[38:39], s[38:39], vcc
	s_and_b64 s[48:49], s[48:49], vcc
	s_or_b64 s[44:45], s[44:45], s[48:49]
.Lk2_l2_4_0:
	s_or_b64 exec, exec, s[46:47]
	v_cmp_lt_u32_e32 vcc, 4, v27
	s_and_saveexec_b64 s[46:47], vcc
	s_cbranch_execz .Lk2_l2_4_1
	v_cvt_f64_f32_e32 v[24:25], v118
	v_cvt_f64_f32_e32 v[30:31], v119
	v_add_f64 v[24:25], v[24:25], -v[74:75]
	v_add_f64 v[30:31], v[30:31], -v[74:75]
	v_add_f64 v[24:25], v[24:25], -v[94:95]
	v_add_f64 v[30:31], v[30:31], -v[98:99]
	v_cmp_le_f64_e32 vcc, s[34:35], v[24:25]
	v_cmp_ge_f64_e64 s[48:49], s[32:33], v[24:25]
	s_or_b64 s[40:41], s[40:41], vcc
	s_and_b64 s[48:49], s[48:49], vcc
	s_or_b64 s[44:45], s[44:45], s[48:49]
	v_cmp_le_f64_e32 vcc, s[34:35], v[30:31]
	v_cmp_ge_f64_e64 s[48:49], s[32:33], v[30:31]
	s_or_b64 s[42:43], s[42:43], vcc
	s_and_b64 s[48:49], s[48:49], vcc
	s_or_b64 s[44:45], s[44:45], s[48:49]
.Lk2_l2_4_1:
	s_or_b64 exec, exec, s[46:47]
	v_cmp_lt_u32_e32 vcc, 5, v28
	s_cbranch_vccz .Lk2_l2_done
	v_cmp_lt_u32_e32 vcc, 5, v26
	s_and_saveexec_b64 s[46:47], vcc
	v_and_b32_e32 v29, 0xffff, v7
	v_lshlrev_b32_e32 v29, 3, v29
	ds_read_b64 v[72:73], v29 offset:12544
	s_mov_b64 exec, s[46:47]
	v_cmp_lt_u32_e32 vcc, 5, v27
	s_and_saveexec_b64 s[46:47], vcc
	v_and_b32_e32 v29, 0xffff, v11
	v_lshlrev_b32_e32 v29, 3, v29
	ds_read_b64 v[74:75], v29 offset:12544
	s_mov_b64 exec, s[46:47]
	s_waitcnt lgkmcnt(0)
	v_cmp_lt_u32_e32 vcc, 5, v26
	s_and_saveexec_b64 s[46:47], vcc
	s_cbranch_execz .Lk2_l2_5_0
	v_cvt_f64_f32_e32 v[24:25], v120
	v_cvt_f64_f32_e32 v[30:31], v121
	v_add_f64 v[24:25], v[24:25], -v[72:73]
	v_add_f64 v[30:31], v[30:31], -v[72:73]
	v_add_f64 v[24:25], v[24:25], -v[92:93]
	v_add_f64 v[30:31], v[30:31], -v[96:97]
	v_cmp_le_f64_e32 vcc, s[34:35], v[24:25]
	v_cmp_ge_f64_e64 s[48:49], s[32:33], v[24:25]
	s_or_b64 s[36:37], s[36:37], vcc
	s_and_b64 s[48:49], s[48:49], vcc
	s_or_b64 s[44:45], s[44:45], s[48:49]
	v_cmp_le_f64_e32 vcc, s[34:35], v[30:31]
	v_cmp_ge_f64_e64 s[48:49], s[32:33], v[30:31]
	s_or_b64 s[38:39], s[38:39], vcc
	s_and_b64 s[48:49], s[48:49], vcc
	s_or_b64 s[44:45], s[44:45], s[48:49]
.Lk2_l2_5_0:
	s_or_b64 exec, exec, s[46:47]
	v_cmp_lt_u32_e32 vcc, 5, v27
	s_and_saveexec_b64 s[46:47], vcc
	s_cbranch_execz .Lk2_l2_5_1
	v_cvt_f64_f32_e32 v[24:25], v122
	v_cvt_f64_f32_e32 v[30:31], v123
	v_add_f64 v[24:25], v[24:25], -v[74:75]
	v_add_f64 v[30:31], v[30:31], -v[74:75]
	v_add_f64 v[24:25], v[24:25], -v[94:95]
	v_add_f64 v[30:31], v[30:31], -v[98:99]
	v_cmp_le_f64_e32 vcc, s[34:35], v[24:25]
	v_cmp_ge_f64_e64 s[48:49], s[32:33], v[24:25]
	s_or_b64 s[40:41], s[40:41], vcc
	s_and_b64 s[48:49], s[48:49], vcc
	s_or_b64 s[44:45], s[44:45], s[48:49]
	v_cmp_le_f64_e32 vcc, s[34:35], v[30:31]
	v_cmp_ge_f64_e64 s[48:49], s[32:33], v[30:31]
	s_or_b64 s[42:43], s[42:43], vcc
	s_and_b64 s[48:49], s[48:49], vcc
	s_or_b64 s[44:45], s[44:45], s[48:49]
.Lk2_l2_5_1:
	s_or_b64 exec, exec, s[46:47]
	v_cmp_lt_u32_e32 vcc, 6, v28
	s_cbranch_vccz .Lk2_l2_done
	v_cmp_lt_u32_e32 vcc, 6, v26
	s_and_saveexec_b64 s[46:47], vcc
	v_lshrrev_b32_e32 v29, 16, v7
	v_lshlrev_b32_e32 v29, 3, v29
	ds_read_b64 v[72:73], v29 offset:12544
	s_mov_b64 exec, s[46:47]
	v_cmp_lt_u32_e32 vcc, 6, v27
	s_and_saveexec_b64 s[46:47], vcc
	v_lshrrev_b32_e32 v29, 16, v11
	v_lshlrev_b32_e32 v29, 3, v29
	ds_read_b64 v[74:75], v29 offset:12544
	s_mov_b64 exec, s[46:47]
	s_waitcnt lgkmcnt(0)
	v_cmp_lt_u32_e32 vcc, 6, v26
	s_and_saveexec_b64 s[46:47], vcc
	s_cbranch_execz .Lk2_l2_6_0
	v_cvt_f64_f32_e32 v[24:25], v124
	v_cvt_f64_f32_e32 v[30:31], v125
	v_add_f64 v[24:25], v[24:25], -v[72:73]
	v_add_f64 v[30:31], v[30:31], -v[72:73]
	v_add_f64 v[24:25], v[24:25], -v[92:93]
	v_add_f64 v[30:31], v[30:31], -v[96:97]
	v_cmp_le_f64_e32 vcc, s[34:35], v[24:25]
	v_cmp_ge_f64_e64 s[48:49], s[32:33], v[24:25]
	s_or_b64 s[36:37], s[36:37], vcc
	s_and_b64 s[48:49], s[48:49], vcc
	s_or_b64 s[44:45], s[44:45], s[48:49]
	v_cmp_le_f64_e32 vcc, s[34:35], v[30:31]
	v_cmp_ge_f64_e64 s[48:49], s[32:33], v[30:31]
	s_or_b64 s[38:39], s[38:39], vcc
	s_and_b64 s[48:49], s[48:49], vcc
	s_or_b64 s[44:45], s[44:45], s[48:49]
.Lk2_l2_6_0:
	s_or_b64 exec, exec, s[46:47]
	v_cmp_lt_u32_e32 vcc, 6, v27
	s_and_saveexec_b64 s[46:47], vcc
	s_cbranch_execz .Lk2_l2_6_1
	v_cvt_f64_f32_e32 v[24:25], v126
	v_cvt_f64_f32_e32 v[30:31], v127
	v_add_f64 v[24:25], v[24:25], -v[74:75]
	v_add_f64 v[30:31], v[30:31], -v[74:75]
	v_add_f64 v[24:25], v[24:25], -v[94:95]
	v_add_f64 v[30:31], v[30:31], -v[98:99]
	v_cmp_le_f64_e32 vcc, s[34:35], v[24:25]
	v_cmp_ge_f64_e64 s[48:49], s[32:33], v[24:25]
	s_or_b64 s[40:41], s[40:41], vcc
	s_and_b64 s[48:49], s[48:49], vcc
	s_or_b64 s[44:45], s[44:45], s[48:49]
	v_cmp_le_f64_e32 vcc, s[34:35], v[30:31]
	v_cmp_ge_f64_e64 s[48:49], s[32:33], v[30:31]
	s_or_b64 s[42:43], s[42:43], vcc
	s_and_b64 s[48:49], s[48:49], vcc
	s_or_b64 s[44:45], s[44:45], s[48:49]

.Lk2_l2_done:
	s_mov_b64 s[76:77], 0
	s_mov_b64 s[94:95], s[36:37]
.Lk2_t15_loop0:
	s_cmp_eq_u64 s[94:95], 0
	s_cbranch_scc1 .Lk2_t15_done0
	s_ff1_i32_b64 s80, s[94:95]
	s_bitset0_b64 s[94:95], s80
	s_bitcmp1_b64 s[38:39], s80
	s_cbranch_scc1 .Lk2_t15_loop0
	s_lshl_b32 s81, s27, 6
	s_add_u32 s81, s81, s80
	s_lshl_b32 s81, s81, 1
	s_lshl_b32 s82, s81, 4
	v_readlane_b32 s83, v16, s80
	v_readlane_b32 s84, v92, s80
	v_readlane_b32 s85, v93, s80
	v_and_b32_e32 v88, 7, v1
	v_bfe_u32 v89, v1, 3, 3
	v_lshlrev_b32_e32 v90, 1, v88
	v_add_u32_e32 v90, s82, v90
	v_mov_b32_e32 v91, s82
	ds_read_u16 v100, v90 offset:22786
	ds_read_u16 v101, v91 offset:22784
	v_mov_b32_e32 v111, s83
	v_mov_b32_e32 v126, s84
	v_mov_b32_e32 v127, s85
	s_waitcnt lgkmcnt(0)
	v_cmp_lt_u32_e64 s[86:87], v88, v101
	s_nop 1
	v_cndmask_b32_e64 v100, 0, v100, s[86:87]
	v_lshlrev_b32_e32 v102, 4, v100
	v_lshl_add_u32 v103, v89, 1, v102
	ds_read_u16 v108, v103 offset:22786
	ds_read_u16 v109, v102 offset:22784
	v_lshlrev_b32_e32 v110, 3, v100
	ds_read_b64 v[112:113], v110 offset:12544
	v_mad_u32_u24 v114, v100, s30, v111
	v_lshlrev_b32_e32 v114, 2, v114
	global_load_dword v115, v114, s[28:29]
	s_waitcnt lgkmcnt(0)
	v_cmp_lt_u32_e64 s[88:89], v89, v109
	s_and_b64 s[88:89], s[88:89], s[86:87]
	v_cndmask_b32_e64 v108, 0, v108, s[88:89]
	v_lshlrev_b32_e32 v116, 3, v108
	ds_read_b64 v[118:119], v116 offset:12544
	v_mad_u32_u24 v117, v108, s30, v111
	v_lshlrev_b32_e32 v117, 2, v117
	global_load_dword v72, v117, s[28:29]
	s_waitcnt vmcnt(0) lgkmcnt(0)
	v_cvt_f64_f32_e32 v[120:121], v115
	v_cvt_f64_f32_e32 v[122:123], v72
	v_add_f64 v[120:121], v[120:121], -v[112:113]
	v_add_f64 v[122:123], v[122:123], -v[118:119]
	v_add_f64 v[124:125], v[120:121], -v[126:127]
	v_add_f64 v[122:123], v[122:123], -v[120:121]
	v_cmp_lt_f64_e64 s[90:91], s[32:33], v[124:125]
	v_cmp_le_f64_e64 s[92:93], s[34:35], v[122:123]
	s_and_b64 s[90:91], s[90:91], s[86:87]
	s_and_b32 s90, s90, 0xff
	s_and_b64 s[92:93], s[92:93], s[88:89]
	s_or_b32 s92, s92, s93
	s_lshr_b32 s93, s92, 16
	s_or_b32 s92, s92, s93
	s_lshr_b32 s93, s92, 8
	s_or_b32 s92, s92, s93
	s_andn2_b32 s90, s90, s92
	s_and_b32 s90, s90, 0xff
	s_cmp_eq_u32 s90, 0
	s_cbranch_scc1 .Lk2_t15_loop0
	s_bitset1_b64 s[76:77], s80
	s_bitset0_b64 s[36:37], s80
	s_branch .Lk2_t15_loop0
.Lk2_t15_done0:
	s_mov_b64 s[78:79], 0
	s_mov_b64 s[94:95], s[40:41]
.Lk2_t15_loop1:
	s_cmp_eq_u64 s[94:95], 0
	s_cbranch_scc1 .Lk2_t15_done1
	s_ff1_i32_b64 s80, s[94:95]
	s_bitset0_b64 s[94:95], s80
	s_bitcmp1_b64 s[42:43], s80
	s_cbranch_scc1 .Lk2_t15_loop1
	s_lshl_b32 s81, s27, 6
	s_add_u32 s81, s81, s80
	s_lshl_b32 s81, s81, 1
	s_add_u32 s81, s81, 1
	s_lshl_b32 s82, s81, 4
	v_readlane_b32 s83, v17, s80
	v_readlane_b32 s84, v94, s80
	v_readlane_b32 s85, v95, s80
	v_and_b32_e32 v88, 7, v1
	v_bfe_u32 v89, v1, 3, 3
	v_lshlrev_b32_e32 v90, 1, v88
	v_add_u32_e32 v90, s82, v90
	v_mov_b32_e32 v91, s82
	ds_read_u16 v100, v90 offset:22786
	ds_read_u16 v101, v91 offset:22784
	v_mov_b32_e32 v111, s83
	v_mov_b32_e32 v126, s84
	v_mov_b32_e32 v127, s85
	s_waitcnt lgkmcnt(0)
	v_cmp_lt_u32_e64 s[86:87], v88, v101
	s_nop 1
	v_cndmask_b32_e64 v100, 0, v100, s[86:87]
	v_lshlrev_b32_e32 v102, 4, v100
	v_lshl_add_u32 v103, v89, 1, v102
	ds_read_u16 v108, v103 offset:22786
	ds_read_u16 v109, v102 offset:22784
	v_lshlrev_b32_e32 v110, 3, v100
	ds_read_b64 v[112:113], v110 offset:12544
	v_mad_u32_u24 v114, v100, s30, v111
	v_lshlrev_b32_e32 v114, 2, v114
	global_load_dword v115, v114, s[28:29]
	s_waitcnt lgkmcnt(0)
	v_cmp_lt_u32_e64 s[88:89], v89, v109
	s_and_b64 s[88:89], s[88:89], s[86:87]
	v_cndmask_b32_e64 v108, 0, v108, s[88:89]
	v_lshlrev_b32_e32 v116, 3, v108
	ds_read_b64 v[118:119], v116 offset:12544
	v_mad_u32_u24 v117, v108, s30, v111
	v_lshlrev_b32_e32 v117, 2, v117
	global_load_dword v72, v117, s[28:29]
	s_waitcnt vmcnt(0) lgkmcnt(0)
	v_cvt_f64_f32_e32 v[120:121], v115
	v_cvt_f64_f32_e32 v[122:123], v72
	v_add_f64 v[120:121], v[120:121], -v[112:113]
	v_add_f64 v[122:123], v[122:123], -v[118:119]
	v_add_f64 v[124:125], v[120:121], -v[126:127]
	v_add_f64 v[122:123], v[122:123], -v[120:121]
	v_cmp_lt_f64_e64 s[90:91], s[32:33], v[124:125]
	v_cmp_le_f64_e64 s[92:93], s[34:35], v[122:123]
	s_and_b64 s[90:91], s[90:91], s[86:87]
	s_and_b32 s90, s90, 0xff
	s_and_b64 s[92:93], s[92:93], s[88:89]
	s_or_b32 s92, s92, s93
	s_lshr_b32 s93, s92, 16
	s_or_b32 s92, s92, s93
	s_lshr_b32 s93, s92, 8
	s_or_b32 s92, s92, s93
	s_andn2_b32 s90, s90, s92
	s_and_b32 s90, s90, 0xff
	s_cmp_eq_u32 s90, 0
	s_cbranch_scc1 .Lk2_t15_loop1
	s_bitset1_b64 s[78:79], s80
	s_bitset0_b64 s[40:41], s80
	s_branch .Lk2_t15_loop1
.Lk2_t15_done1:
	s_or_b64 s[48:49], s[76:77], s[78:79]
	s_cmp_eq_u64 s[48:49], 0
	s_cbranch_scc1 .Lk2_nochg
	s_mov_b64 exec, s[76:77]
	ds_write_b64 v2, v[96:97] offset:0
	ds_write_b32 v104, v14 offset:4096
	s_mov_b64 exec, s[78:79]
	ds_write_b64 v2, v[98:99] offset:8
	ds_write_b32 v104, v15 offset:4100
	s_mov_b64 exec, -1
	v_mov_b32_e32 v30, 1
	ds_write_b32 v105, v30 offset:28
.Lk2_nochg:
	v_cmp_lt_u32_e32 vcc, 7, v28
	s_or_b64 s[48:49], vcc, s[44:45]
	s_cmp_eq_u64 s[48:49], 0
	s_cbranch_scc1 .Lk2_nofb
	v_mov_b32_e32 v30, 1
	ds_write_b32 v105, v30 offset:8

.Lk2_nohard:
	s_waitcnt lgkmcnt(0)
	s_barrier
	ds_read_b128 v[88:91], v105
	ds_read_b32 v100, v105 offset:28
	s_waitcnt lgkmcnt(0)
	v_readfirstlane_b32 s31, v90
	v_readfirstlane_b32 s74, v88
	v_readfirstlane_b32 s99, v100
	s_cmp_lg_u32 s31, 0
	s_cbranch_scc1 .Lk2_fallback
	s_cmp_lg_u32 s74, 0
	s_cbranch_scc1 .Lk2_hard
	s_cmp_lg_u32 s99, 0
	s_cbranch_scc1 .Lk2_rerank
.Lk2_late:
	s_cmp_lt_u32 s54, 0x64
	s_cbranch_scc0 .Lk2_lg1_skip
	s_cmp_eq_u32 s96, 0
	s_cbranch_scc0 .Lk2_lg1_skip
	global_load_dwordx4 v[32:35], v69, s[64:65] offset:0 nt
	global_load_dwordx4 v[36:39], v69, s[64:65] offset:1024 nt
	global_load_dwordx4 v[40:43], v69, s[64:65] offset:2048 nt
	global_load_dwordx4 v[44:47], v69, s[64:65] offset:3072 nt
	global_load_dwordx4 v[48:51], v70, s[64:65] offset:0 nt
	global_load_dwordx4 v[52:55], v70, s[64:65] offset:1024 nt
	global_load_dwordx4 v[56:59], v70, s[64:65] offset:2048 nt
	global_load_dwordx4 v[60:63], v70, s[64:65] offset:3072 nt

.Lk2_rerank:
	v_lshrrev_b32_e32 v29, 5, v1
	v_and_b32_e32 v31, 31, v1
	v_lshl_add_u32 v29, s25, 3, v29
	v_lshlrev_b32_e32 v29, 3, v29
	v_lshlrev_b32_e32 v31, 3, v31
	ds_read_b64 v[64:65], v29 offset:0
	ds_read_b64 v[88:89], v31 offset:0
	ds_read_b64 v[90:91], v31 offset:256
	ds_read_b64 v[100:101], v31 offset:512
	ds_read_b64 v[102:103], v31 offset:768
	ds_read_b64 v[108:109], v31 offset:1024
	ds_read_b64 v[110:111], v31 offset:1280
	ds_read_b64 v[112:113], v31 offset:1536
	ds_read_b64 v[114:115], v31 offset:1792
	ds_read_b64 v[116:117], v31 offset:2048
	ds_read_b64 v[118:119], v31 offset:2304
	ds_read_b64 v[120:121], v31 offset:2560
	ds_read_b64 v[122:123], v31 offset:2816
	ds_read_b64 v[124:125], v31 offset:3072
	v_mov_b32_e32 v66, 0
	v_mov_b32_e32 v67, 0
	s_waitcnt lgkmcnt(12)
	ds_read_b64 v[126:127], v31 offset:3328
	v_add_f64 v[24:25], v[88:89], -v[64:65]
	v_cmp_lt_f64_e32 vcc, s[32:33], v[24:25]
	v_cmp_ge_f64_e64 s[48:49], s[32:33], |v[24:25]|
	s_nop 0
	v_addc_co_u32_e32 v66, vcc, 0, v66, vcc
	v_addc_co_u32_e64 v67, s[50:51], 0, v67, s[48:49]
	s_waitcnt lgkmcnt(12)
	ds_read_b64 v[72:73], v31 offset:3584
	v_add_f64 v[24:25], v[90:91], -v[64:65]
	v_cmp_lt_f64_e32 vcc, s[32:33], v[24:25]
	v_cmp_ge_f64_e64 s[48:49], s[32:33], |v[24:25]|
	s_nop 0
	v_addc_co_u32_e32 v66, vcc, 0, v66, vcc
	v_addc_co_u32_e64 v67, s[50:51], 0, v67, s[48:49]
	s_waitcnt lgkmcnt(12)
	ds_read_b64 v[74:75], v31 offset:3840
	v_add_f64 v[24:25], v[100:101], -v[64:65]
	v_cmp_lt_f64_e32 vcc, s[32:33], v[24:25]
	v_cmp_ge_f64_e64 s[48:49], s[32:33], |v[24:25]|
	s_nop 0
	v_addc_co_u32_e32 v66, vcc, 0, v66, vcc
	v_addc_co_u32_e64 v67, s[50:51], 0, v67, s[48:49]
	s_waitcnt lgkmcnt(12)
	v_add_f64 v[24:25], v[102:103], -v[64:65]
	v_cmp_lt_f64_e32 vcc, s[32:33], v[24:25]
	v_cmp_ge_f64_e64 s[48:49], s[32:33], |v[24:25]|
	s_nop 0
	v_addc_co_u32_e32 v66, vcc, 0, v66, vcc
	v_addc_co_u32_e64 v67, s[50:51], 0, v67, s[48:49]
	s_waitcnt lgkmcnt(11)
	v_add_f64 v[24:25], v[108:109], -v[64:65]
	v_cmp_lt_f64_e32 vcc, s[32:33], v[24:25]
	v_cmp_ge_f64_e64 s[48:49], s[32:33], |v[24:25]|
	s_nop 0
	v_addc_co_u32_e32 v66, vcc, 0, v66, vcc
	v_addc_co_u32_e64 v67, s[50:51], 0, v67, s[48:49]
	s_waitcnt lgkmcnt(10)
	v_add_f64 v[24:25], v[110:111], -v[64:65]
	v_cmp_lt_f64_e32 vcc, s[32:33], v[24:25]
	v_cmp_ge_f64_e64 s[48:49], s[32:33], |v[24:25]|
	s_nop 0
	v_addc_co_u32_e32 v66, vcc, 0, v66, vcc
	v_addc_co_u32_e64 v67, s[50:51], 0, v67, s[48:49]
	s_waitcnt lgkmcnt(9)
	v_add_f64 v[24:25], v[112:113], -v[64:65]
	v_cmp_lt_f64_e32 vcc, s[32:33], v[24:25]
	v_cmp_ge_f64_e64 s[48:49], s[32:33], |v[24:25]|
	s_nop 0
	v_addc_co_u32_e32 v66, vcc, 0, v66, vcc
	v_addc_co_u32_e64 v67, s[50:51], 0, v67, s[48:49]
	s_waitcnt lgkmcnt(8)
	v_add_f64 v[24:25], v[114:115], -v[64:65]
	v_cmp_lt_f64_e32 vcc, s[32:33], v[24:25]
	v_cmp_ge_f64_e64 s[48:49], s[32:33], |v[24:25]|
	s_nop 0
	v_addc_co_u32_e32 v66, vcc, 0, v66, vcc
	v_addc_co_u32_e64 v67, s[50:51], 0, v67, s[48:49]
	s_waitcnt lgkmcnt(7)
	v_add_f64 v[24:25], v[116:117], -v[64:65]
	v_cmp_lt_f64_e32 vcc, s[32:33], v[24:25]
	v_cmp_ge_f64_e64 s[48:49], s[32:33], |v[24:25]|
	s_nop 0
	v_addc_co_u32_e32 v66, vcc, 0, v66, vcc
	v_addc_co_u32_e64 v67, s[50:51], 0, v67, s[48:49]
	s_waitcnt lgkmcnt(6)
	v_add_f64 v[24:25], v[118:119], -v[64:65]
	v_cmp_lt_f64_e32 vcc, s[32:33], v[24:25]
	v_cmp_ge_f64_e64 s[48:49], s[32:33], |v[24:25]|
	s_nop 0
	v_addc_co_u32_e32 v66, vcc, 0, v66, vcc
	v_addc_co_u32_e64 v67, s[50:51], 0, v67, s[48:49]
	s_waitcnt lgkmcnt(5)
	v_add_f64 v[24:25], v[120:121], -v[64:65]
	v_cmp_lt_f64_e32 vcc, s[32:33], v[24:25]
	v_cmp_ge_f64_e64 s[48:49], s[32:33], |v[24:25]|
	s_nop 0
	v_addc_co_u32_e32 v66, vcc, 0, v66, vcc
	v_addc_co_u32_e64 v67, s[50:51], 0, v67, s[48:49]
	s_waitcnt lgkmcnt(4)
	v_add_f64 v[24:25], v[122:123], -v[64:65]
	v_cmp_lt_f64_e32 vcc, s[32:33], v[24:25]
	v_cmp_ge_f64_e64 s[48:49], s[32:33], |v[24:25]|
	s_nop 0
	v_addc_co_u32_e32 v66, vcc, 0, v66, vcc
	v_addc_co_u32_e64 v67, s[50:51], 0, v67, s[48:49]
	s_waitcnt lgkmcnt(3)
	v_add_f64 v[24:25], v[124:125], -v[64:65]
	v_cmp_lt_f64_e32 vcc, s[32:33], v[24:25]
	v_cmp_ge_f64_e64 s[48:49], s[32:33], |v[24:25]|
	s_nop 0
	v_addc_co_u32_e32 v66, vcc, 0, v66, vcc
	v_addc_co_u32_e64 v67, s[50:51], 0, v67, s[48:49]
	s_waitcnt lgkmcnt(2)
	v_add_f64 v[24:25], v[126:127], -v[64:65]
	v_cmp_lt_f64_e32 vcc, s[32:33], v[24:25]
	v_cmp_ge_f64_e64 s[48:49], s[32:33], |v[24:25]|
	s_nop 0
	v_addc_co_u32_e32 v66, vcc, 0, v66, vcc
	v_addc_co_u32_e64 v67, s[50:51], 0, v67, s[48:49]
	s_waitcnt lgkmcnt(1)
	v_add_f64 v[24:25], v[72:73], -v[64:65]
	v_cmp_lt_f64_e32 vcc, s[32:33], v[24:25]
	v_cmp_ge_f64_e64 s[48:49], s[32:33], |v[24:25]|
	s_nop 0
	v_addc_co_u32_e32 v66, vcc, 0, v66, vcc
	v_addc_co_u32_e64 v67, s[50:51], 0, v67, s[48:49]
	s_waitcnt lgkmcnt(0)
	v_add_f64 v[24:25], v[74:75], -v[64:65]
	v_cmp_lt_f64_e32 vcc, s[32:33], v[24:25]
	v_cmp_ge_f64_e64 s[48:49], s[32:33], |v[24:25]|
	s_nop 0
	v_addc_co_u32_e32 v66, vcc, 0, v66, vcc
	v_addc_co_u32_e64 v67, s[50:51], 0, v67, s[48:49]
	v_lshl_or_b32 v68, v67, 16, v66
	s_nop 1
	v_add_u32_dpp v68, v68, v68 quad_perm:[1,0,3,2] row_mask:0xf bank_mask:0xf
	s_nop 1
	v_add_u32_dpp v68, v68, v68 quad_perm:[2,3,0,1] row_mask:0xf bank_mask:0xf
	s_nop 1
	v_add_u32_dpp v68, v68, v68 row_half_mirror row_mask:0xf bank_mask:0xf
	s_nop 1
	v_add_u32_dpp v68, v68, v68 row_mirror row_mask:0xf bank_mask:0xf
	s_nop 1
	v_add_u32_dpp v68, v68, v68 row_bcast:15 row_mask:0xa bank_mask:0xf
	s_nop 1
	v_readlane_b32 s52, v68, 31
	v_readlane_b32 s53, v68, 63
	s_and_b32 s54, s52, 0xffff
	s_lshr_b32 s55, s52, 16
	s_and_b32 s56, s53, 0xffff
	s_lshr_b32 s57, s53, 16
	s_cmp_gt_u32 s55, 1
	s_cselect_b32 s58, 1, 0
	s_cmp_lt_u32 s54, 0x64
	s_cselect_b32 s59, 1, 0
	s_and_b32 s58, s58, s59
	s_cmp_gt_u32 s57, 1
	s_cselect_b32 s60, 1, 0
	s_cmp_lt_u32 s56, 0x64
	s_cselect_b32 s61, 1, 0
	s_and_b32 s60, s60, s61
	s_or_b32 s61, s58, s60
	s_cmp_eq_u32 s97, 0
	s_cbranch_scc1 .Lk2_late
	s_mov_b32 s3, s54
	s_mov_b32 s54, s56
	s_mov_b32 s56, s3
	s_mov_b32 s3, s55
	s_mov_b32 s55, s57
	s_mov_b32 s57, s3
	s_mov_b32 s3, s58
	s_mov_b32 s58, s60
	s_mov_b32 s60, s3
	s_branch .Lk2_late
.Lk2_needref:
	s_cmp_eq_u32 s97, 0
	s_cselect_b32 s48, s58, s60
	s_cselect_b32 s49, s60, s58
	s_cmp_lg_u32 s48, 0
	s_cselect_b32 s48, -1, 0
	s_cmp_lg_u32 s49, 0
	s_cselect_b32 s49, -1, 0
	s_mov_b64 exec, s[48:49]
	v_and_b32_e32 v29, 31, v1
	v_lshlrev_b32_e32 v30, 2, v29
	v_lshlrev_b32_e32 v29, 3, v29
	v_mov_b32_e32 v31, 1
	s_mov_b32 s3, 4

.Lk2_rf_nopf:
	v_add_f64 v[120:121], v[120:121], -v[118:119]
	v_add_f64 v[116:117], v[116:117], -v[118:119]
	v_mul_f64 v[122:123], v[120:121], s[74:75]
	v_mul_f64 v[112:113], v[116:117], s[74:75]
	v_rndne_f64_e32 v[122:123], v[122:123]
	v_rndne_f64_e32 v[112:113], v[112:113]
	v_fma_f64 v[120:121], v[122:123], s[76:77], v[120:121]
	v_fma_f64 v[116:117], v[112:113], s[76:77], v[116:117]
	v_fma_f64 v[120:121], v[122:123], s[78:79], v[120:121]
	v_fma_f64 v[116:117], v[112:113], s[78:79], v[116:117]
	v_fma_f64 v[124:125], v[108:109], v[120:121], s[80:81]
	v_fma_f64 v[64:65], v[108:109], v[116:117], s[80:81]
	v_fma_f64 v[124:125], v[124:125], v[120:121], s[82:83]
	v_fma_f64 v[64:65], v[64:65], v[116:117], s[82:83]
	v_fma_f64 v[124:125], v[124:125], v[120:121], s[84:85]
	v_fma_f64 v[64:65], v[64:65], v[116:117], s[84:85]
	v_fma_f64 v[124:125], v[124:125], v[120:121], s[86:87]
	v_fma_f64 v[64:65], v[64:65], v[116:117], s[86:87]
	v_fma_f64 v[124:125], v[124:125], v[120:121], s[88:89]
	v_fma_f64 v[64:65], v[64:65], v[116:117], s[88:89]
	v_fma_f64 v[124:125], v[124:125], v[120:121], s[90:91]
	v_fma_f64 v[64:65], v[64:65], v[116:117], s[90:91]
	v_fma_f64 v[124:125], v[124:125], v[120:121], s[92:93]
	v_fma_f64 v[64:65], v[64:65], v[116:117], s[92:93]
	v_fma_f64 v[124:125], v[124:125], v[120:121], s[94:95]
	v_fma_f64 v[64:65], v[64:65], v[116:117], s[94:95]
	v_fma_f64 v[124:125], v[124:125], v[120:121], 0.5
	v_fma_f64 v[64:65], v[64:65], v[116:117], 0.5
	v_fma_f64 v[124:125], v[124:125], v[120:121], 1.0
	v_fma_f64 v[64:65], v[64:65], v[116:117], 1.0
	v_fma_f64 v[124:125], v[124:125], v[120:121], 1.0
	v_fma_f64 v[64:65], v[64:65], v[116:117], 1.0
	v_cvt_i32_f64_e32 v126, v[122:123]
	v_cvt_i32_f64_e32 v68, v[112:113]
	v_ldexp_f64 v[124:125], v[124:125], v126
	v_ldexp_f64 v[64:65], v[64:65], v68
	v_add_f64 v[110:111], v[110:111], v[124:125]
	v_add_f64 v[66:67], v[66:67], v[64:65]
	s_sub_u32 s3, s3, 1
	s_cmp_lg_u32 s3, 0
	s_cbranch_scc1 .Lk2_rf_exp
	s_waitcnt lgkmcnt(0)
	v_cvt_f64_f32_e32 v[120:121], v30
	v_add_f64 v[120:121], v[120:121], -v[118:119]
	v_mul_f64 v[122:123], v[120:121], s[74:75]
	v_rndne_f64_e32 v[122:123], v[122:123]
	v_fma_f64 v[120:121], v[122:123], s[76:77], v[120:121]
	v_fma_f64 v[120:121], v[122:123], s[78:79], v[120:121]
	v_fma_f64 v[124:125], v[108:109], v[120:121], s[80:81]
	v_fma_f64 v[124:125], v[124:125], v[120:121], s[82:83]
	v_fma_f64 v[124:125], v[124:125], v[120:121], s[84:85]
	v_fma_f64 v[124:125], v[124:125], v[120:121], s[86:87]
	v_fma_f64 v[124:125], v[124:125], v[120:121], s[88:89]
	v_fma_f64 v[124:125], v[124:125], v[120:121], s[90:91]
	v_fma_f64 v[124:125], v[124:125], v[120:121], s[92:93]
	v_fma_f64 v[124:125], v[124:125], v[120:121], s[94:95]
	v_fma_f64 v[124:125], v[124:125], v[120:121], 0.5
	v_fma_f64 v[124:125], v[124:125], v[120:121], 1.0
	v_fma_f64 v[124:125], v[124:125], v[120:121], 1.0
	v_cvt_i32_f64_e32 v126, v[122:123]
	v_ldexp_f64 v[124:125], v[124:125], v126
	v_add_f64 v[110:111], v[110:111], v[124:125]
	v_add_f64 v[110:111], v[110:111], v[66:67]
	s_nop 1
	v_mov_b32_dpp v126, v110 quad_perm:[1,0,3,2] row_mask:0xf bank_mask:0xf
	v_mov_b32_dpp v127, v111 quad_perm:[1,0,3,2] row_mask:0xf bank_mask:0xf
	v_add_f64 v[110:111], v[110:111], v[126:127]
	s_nop 1
	v_mov_b32_dpp v126, v110 quad_perm:[2,3,0,1] row_mask:0xf bank_mask:0xf
	v_mov_b32_dpp v127, v111 quad_perm:[2,3,0,1] row_mask:0xf bank_mask:0xf
	v_add_f64 v[110:111], v[110:111], v[126:127]
	s_nop 1
	v_mov_b32_dpp v126, v110 row_half_mirror row_mask:0xf bank_mask:0xf
	v_mov_b32_dpp v127, v111 row_half_mirror row_mask:0xf bank_mask:0xf
	v_add_f64 v[110:111], v[110:111], v[126:127]
	s_nop 1
	v_mov_b32_dpp v126, v110 row_mirror row_mask:0xf bank_mask:0xf
	v_mov_b32_dpp v127, v111 row_mirror row_mask:0xf bank_mask:0xf
	v_add_f64 v[110:111], v[110:111], v[126:127]
	s_nop 1
	v_readlane_b32 s52, v110, 15
	v_readlane_b32 s53, v111, 15
	v_readlane_b32 s44, v110, 31
	v_readlane_b32 s45, v111, 31
	v_readlane_b32 s50, v110, 47
	v_readlane_b32 s51, v111, 47
	v_readlane_b32 s46, v110, 63
	v_readlane_b32 s47, v111, 63
	v_add_f64 v[110:111], s[52:53], 0
	v_add_f64 v[110:111], v[110:111], s[44:45]
	v_add_f64 v[110:111], v[110:111], s[50:51]
	v_add_f64 v[110:111], v[110:111], s[46:47]
	v_cvt_f64_f32_e32 v[120:121], s49
	v_add_f64 v[120:121], v[120:121], -v[118:119]
	v_mul_f64 v[122:123], v[120:121], s[74:75]
	v_rndne_f64_e32 v[122:123], v[122:123]
	v_fma_f64 v[120:121], v[122:123], s[76:77], v[120:121]
	v_fma_f64 v[120:121], v[122:123], s[78:79], v[120:121]
	v_fma_f64 v[124:125], v[108:109], v[120:121], s[80:81]
	v_fma_f64 v[124:125], v[124:125], v[120:121], s[82:83]
	v_fma_f64 v[124:125], v[124:125], v[120:121], s[84:85]
	v_fma_f64 v[124:125], v[124:125], v[120:121], s[86:87]
	v_fma_f64 v[124:125], v[124:125], v[120:121], s[88:89]
	v_fma_f64 v[124:125], v[124:125], v[120:121], s[90:91]
	v_fma_f64 v[124:125], v[124:125], v[120:121], s[92:93]
	v_fma_f64 v[124:125], v[124:125], v[120:121], s[94:95]
	v_fma_f64 v[124:125], v[124:125], v[120:121], 0.5
	v_fma_f64 v[124:125], v[124:125], v[120:121], 1.0
	v_fma_f64 v[124:125], v[124:125], v[120:121], 1.0
	v_cvt_i32_f64_e32 v126, v[122:123]
	v_ldexp_f64 v[124:125], v[124:125], v126
	v_add_f64 v[110:111], v[110:111], v[124:125]
	v_cvt_f32_f64_e32 v126, v[110:111]
	v_log_f32_e32 v126, v126
	s_nop 0
	v_mul_f32_e32 v126, 0x3f317218, v126
	v_cvt_f64_f32_e32 v[112:113], v126
	s_mov_b32 s3, 2

.Lk2_rc_loop:
	ds_read_b64 v[116:117], v30 offset:0
	ds_read_b64 v[118:119], v30 offset:256
	ds_read_b64 v[120:121], v30 offset:512
	ds_read_b64 v[122:123], v30 offset:768
	s_waitcnt lgkmcnt(0)
	v_cmp_gt_f64_e32 vcc, v[116:117], v[64:65]
	v_cmp_eq_f64_e64 s[48:49], v[116:117], v[64:65]
	v_cmp_lt_u32_e64 s[50:51], v31, v29
	s_and_b64 s[48:49], s[48:49], s[50:51]
	s_or_b64 s[48:49], s[48:49], vcc
	v_addc_co_u32_e64 v66, s[50:51], 0, v66, s[48:49]
	v_add_u32_e32 v28, 32, v31
	v_cmp_gt_f64_e32 vcc, v[118:119], v[64:65]
	v_cmp_eq_f64_e64 s[48:49], v[118:119], v[64:65]
	v_cmp_lt_u32_e64 s[50:51], v28, v29
	s_and_b64 s[48:49], s[48:49], s[50:51]
	s_or_b64 s[48:49], s[48:49], vcc
	v_addc_co_u32_e64 v66, s[50:51], 0, v66, s[48:49]
	v_add_u32_e32 v28, 64, v31
	v_cmp_gt_f64_e32 vcc, v[120:121], v[64:65]
	v_cmp_eq_f64_e64 s[48:49], v[120:121], v[64:65]
	v_cmp_lt_u32_e64 s[50:51], v28, v29
	s_and_b64 s[48:49], s[48:49], s[50:51]
	s_or_b64 s[48:49], s[48:49], vcc
	v_addc_co_u32_e64 v66, s[50:51], 0, v66, s[48:49]
	v_add_u32_e32 v28, 96, v31
	v_cmp_gt_f64_e32 vcc, v[122:123], v[64:65]
	v_cmp_eq_f64_e64 s[48:49], v[122:123], v[64:65]
	v_cmp_lt_u32_e64 s[50:51], v28, v29
	s_and_b64 s[48:49], s[48:49], s[50:51]
	s_or_b64 s[48:49], s[48:49], vcc
	v_addc_co_u32_e64 v66, s[50:51], 0, v66, s[48:49]
	v_add_u32_e32 v30, 0x400, v30
	v_add_u32_e32 v31, 0x80, v31
	s_sub_u32 s3, s3, 1
	s_cmp_lg_u32 s3, 0
	s_cbranch_scc1 .Lk2_rc_loop
	s_nop 1
	v_add_u32_dpp v66, v66, v66 quad_perm:[1,0,3,2] row_mask:0xf bank_mask:0xf
	s_nop 1
	v_add_u32_dpp v66, v66, v66 quad_perm:[2,3,0,1] row_mask:0xf bank_mask:0xf
	s_nop 1
	v_add_u32_dpp v66, v66, v66 row_half_mirror row_mask:0xf bank_mask:0xf
	s_nop 1
	v_add_u32_dpp v66, v66, v66 row_mirror row_mask:0xf bank_mask:0xf
	s_nop 1
	v_add_u32_dpp v66, v66, v66 row_bcast:15 row_mask:0xa bank_mask:0xf
	s_nop 1
	v_readlane_b32 s52, v66, 31
	v_readlane_b32 s53, v66, 63
	s_cmp_eq_u32 s97, 0
	s_cselect_b32 s3, s52, s53
	s_cselect_b32 s53, s53, s52
	s_mov_b32 s52, s3
	s_cmp_lg_u32 s58, 0
	s_cselect_b32 s54, s52, s54
	s_cmp_lg_u32 s60, 0
	s_cselect_b32 s56, s53, s56
	s_waitcnt vmcnt(0)
	s_branch .Lk2_dst_stores
